# v22 = v20 but the 4 loader waves of a workgroup convert 4 consecutive k-blocks of one n-block (256 contiguous output bytes per row)
# speedup vs baseline: 1.0015x; 1.0015x over previous
; __device__ __forceinline__ ConvTile conv_tile_desc(const unsigned long long* tab, int t) {
;     ...
;     else if (t < CT_C) { const int u = t - CT_B; e = u / 14336; const int v = u % 14336; si = 7; di = 16; N = EXD; K = DM; nb = v % 224; kb = v / 224; mode = 1; }
;     else { const int u = (t < CT_TOTAL ? t : CT_TOTAL - 1) - CT_C; e = u / 7168; const int v = u % 7168; si = 9; di = 17; N = DM; K = EXD; nb = v & 31; kb = v >> 5; }
;     const int n0 = nb * 64;
;     int col0 = n0, nvalid = 64;
;     if (mode) { col0 = (n0 >> 8) * 128 + (n0 & 127); si += (n0 >> 7) & 1; }
.LBB0_637:
	s_andn2_b64 vcc, exec, s[56:57]
	s_mov_b64 s[62:63], 0
	s_cbranch_vccnz .LBB0_746
	s_add_i32 s56, s72, 0xffff7b00
	s_lshr_b32 s57, s56, 11
	s_mul_hi_u32 s74, s57, 0x24924925
	s_mul_i32 s57, s74, 0x3800
	s_sub_i32 s56, s56, s57
	s_and_b32 s65, s56, 3
	s_lshr_b32 s56, s56, 2
	s_bfe_u32 s57, s56, 0x100005
	s_mulk_i32 s57, 0x2493
	s_lshr_b32 s64, s57, 16
	s_mul_i32 s57, s64, 0xe0
	s_sub_i32 s56, s56, s57
	s_lshl_b32 s64, s64, 2
	s_or_b32 s64, s64, s65
	s_mov_b32 s75, 16
	s_and_b32 s65, s56, 0xffff
	s_mov_b64 s[60:61], 1
	s_mov_b64 s[56:57], 0x800
	s_movk_i32 s96, 0x1c00

; __device__ __forceinline__ ConvTile conv_tile_desc(const unsigned long long* tab, int t) {
;     ...
;     else if (t < CT_C) { const int u = t - CT_B; e = u / 14336; const int v = u % 14336; si = 7; di = 16; N = EXD; K = DM; nb = v % 224; kb = v / 224; mode = 1; }
;     else { const int u = (t < CT_TOTAL ? t : CT_TOTAL - 1) - CT_C; e = u / 7168; const int v = u % 7168; si = 9; di = 17; N = DM; K = EXD; nb = v & 31; kb = v >> 5; }
;     const int n0 = nb * 64;
;     int col0 = n0, nvalid = 64;
;     if (mode) { col0 = (n0 >> 8) * 128 + (n0 & 127); si += (n0 >> 7) & 1; }
.LBB0_664:
	s_andn2_b64 vcc, exec, s[56:57]
	s_cbranch_vccnz .LBB0_747
	s_add_i32 s56, s72, 0xffff7b00
	s_lshr_b32 s57, s56, 11
	s_mul_hi_u32 s64, s57, 0x24924925
	s_mul_i32 s57, s64, 0x3800
	s_sub_i32 s56, s56, s57
	s_and_b32 s75, s56, 3
	s_lshr_b32 s56, s56, 2
	s_bfe_u32 s57, s56, 0x100005
	s_mulk_i32 s57, 0x2493
	s_lshr_b32 s74, s57, 16
	s_mul_i32 s57, s74, 0xe0
	s_sub_i32 s56, s56, s57
	s_lshl_b32 s74, s74, 2
	s_or_b32 s74, s74, s75
	s_and_b32 s75, s56, 0xffff
	s_mov_b64 s[60:61], 0
	s_mov_b64 s[62:63], 0x800
	s_movk_i32 s56, 0x1c00
	s_mov_b32 s57, 7
	s_mov_b64 s[96:97], 0
